# P5: next unit's two hg_gates parameters loaded with the mid-unit prefetch; no in-order wait at the unit start; own HBM loads waited at the epilogue
# baseline (speedup 1.0000x reference)
.LBB0_520:
	s_cmp_gt_i32 s78, 5
	s_cselect_b64 s[0:1], -1, 0
	s_cmp_lt_i32 s79, 6
	s_cselect_b64 s[4:5], -1, 0
	s_or_b64 s[0:1], s[0:1], s[4:5]
	s_and_b64 vcc, exec, s[0:1]
	s_cbranch_vccnz .LBB0_593
	s_lshl_b32 s0, s2, 3
	s_and_b32 s0, s0, 0xfffffc00
	s_and_b32 s1, s2, 0x7f
	v_writelane_b32 v254, s94, 8
	s_waitcnt lgkmcnt(0)
	s_or_b32 s61, s0, s1
	s_cmpk_lt_i32 s2, 0x100
	v_writelane_b32 v254, s95, 9
	v_writelane_b32 v254, s93, 10
	s_cselect_b32 s6, s61, 0x800
	v_writelane_b32 v254, s92, 11
	s_cmpk_gt_i32 s6, 0x7ff
	v_writelane_b32 v254, s91, 12
	s_cbranch_scc1 .LBB0_539
	s_add_u32 s4, s76, 0x4c5e8000
	s_addc_u32 s5, s77, 0
	s_ashr_i32 s8, s6, 10
	s_add_u32 s0, s76, 0x364e8000
	s_addc_u32 s1, s77, 0
	s_ashr_i32 s9, s8, 31
	s_lshl_b32 s3, s6, 6
	s_waitcnt vmcnt(0)
	v_lshrrev_b32_e32 v72, 3, v0
	v_mov_b32_e32 v1, 0x1ff0
	s_lshl_b64 s[8:9], s[8:9], 13
	v_bitop3_b32 v1, s3, v1, v72 bitop3:0xc8
	v_or_b32_e32 v1, s8, v1
	s_movk_i32 s3, 0x3800
	v_mov_b64_e32 v[2:3], s[0:1]
	v_and_b32_e32 v70, 0x7f, v0
	v_mad_u64_u32 v[2:3], s[10:11], v1, s3, v[2:3]
	v_mov_b32_e32 v73, 0x3800
	v_mad_i32_i24 v3, s9, v73, v3
	v_mov_b32_e32 v75, 0
	v_lshlrev_b32_e32 v74, 1, v70
	v_lshl_add_u64 v[8:9], v[2:3], 0, v[74:75]
	s_movk_i32 s7, 0x2000
	v_add_co_u32_e32 v10, vcc, s7, v8
	s_movk_i32 s7, 0x5000
	s_nop 0
	v_addc_co_u32_e32 v11, vcc, 0, v9, vcc
	v_add_co_u32_e32 v2, vcc, s7, v8
	s_mov_b32 s7, 0x9000
	s_nop 0
	v_addc_co_u32_e32 v3, vcc, 0, v9, vcc
	v_add_co_u32_e32 v14, vcc, s7, v8
	s_mov_b32 s7, 0xc000
	s_nop 0
	v_addc_co_u32_e32 v15, vcc, 0, v9, vcc
	global_load_ushort v1, v[10:11], off
	global_load_ushort v20, v[2:3], off offset:2048
	v_add_co_u32_e32 v2, vcc, s7, v8
	s_mov_b32 s7, 0x10000
	s_nop 0
	v_addc_co_u32_e32 v3, vcc, 0, v9, vcc
	v_add_co_u32_e32 v4, vcc, s7, v8
	s_mov_b32 s7, 0x13000
	s_nop 0
	v_addc_co_u32_e32 v5, vcc, 0, v9, vcc
	global_load_ushort v21, v[14:15], off
	global_load_ushort v22, v[2:3], off offset:2048
	v_add_co_u32_e32 v2, vcc, s7, v8
	s_mov_b32 s7, 0x17000
	s_nop 0
	v_addc_co_u32_e32 v3, vcc, 0, v9, vcc
	v_add_co_u32_e32 v12, vcc, s7, v8
	s_mov_b32 s7, 0x1a000
	s_nop 0
	v_addc_co_u32_e32 v13, vcc, 0, v9, vcc
	global_load_ushort v24, v[2:3], off offset:2048
	global_load_ushort v25, v[12:13], off
	v_add_co_u32_e32 v2, vcc, s7, v8
	s_mov_b32 s7, 0x1e000
	s_nop 0
	v_addc_co_u32_e32 v3, vcc, 0, v9, vcc
	global_load_ushort v50, v[2:3], off offset:2048
	v_add_co_u32_e32 v2, vcc, s7, v8
	s_mov_b32 s7, 0x21000
	s_nop 0
	v_addc_co_u32_e32 v3, vcc, 0, v9, vcc
	v_add_co_u32_e32 v6, vcc, s7, v8
	s_mov_b32 s7, 0x25000
	s_nop 0
	v_addc_co_u32_e32 v7, vcc, 0, v9, vcc
	global_load_ushort v52, v[6:7], off offset:2048
	v_add_co_u32_e32 v6, vcc, s7, v8
	s_mov_b32 s7, 0x28000
	s_nop 0
	v_addc_co_u32_e32 v7, vcc, 0, v9, vcc
	v_add_co_u32_e32 v16, vcc, s7, v8
	s_mov_b32 s7, 0x2c000
	s_nop 0
	v_addc_co_u32_e32 v17, vcc, 0, v9, vcc
	global_load_ushort v54, v[16:17], off offset:2048
	v_add_co_u32_e32 v16, vcc, s7, v8
	s_mov_b32 s7, 0x2f000
	s_nop 0
	v_addc_co_u32_e32 v17, vcc, 0, v9, vcc
	v_add_co_u32_e32 v18, vcc, s7, v8
	s_mov_b32 s7, 0x33000
	s_nop 0
	v_addc_co_u32_e32 v19, vcc, 0, v9, vcc
	global_load_ushort v56, v[18:19], off offset:2048
	v_add_co_u32_e32 v18, vcc, s7, v8
	s_mov_b32 s7, 0x36000
	s_nop 0
	v_addc_co_u32_e32 v19, vcc, 0, v9, vcc
	v_add_co_u32_e32 v26, vcc, s7, v8
	s_movk_i32 s72, 0x1000
	s_nop 0
	v_addc_co_u32_e32 v27, vcc, 0, v9, vcc
	global_load_ushort v58, v[26:27], off offset:2048
	v_add_co_u32_e32 v26, vcc, s72, v8
	s_movk_i32 s7, 0x6000
	s_nop 0
	v_addc_co_u32_e32 v27, vcc, 0, v9, vcc
	global_load_ushort v59, v[26:27], off offset:2048
	v_add_co_u32_e32 v26, vcc, s7, v8
	s_mov_b32 s7, 0x8000
	s_nop 0
	v_addc_co_u32_e32 v27, vcc, 0, v9, vcc
	v_add_co_u32_e32 v28, vcc, s7, v8
	s_mov_b32 s7, 0xd000
	s_nop 0
	v_addc_co_u32_e32 v29, vcc, 0, v9, vcc
	global_load_ushort v61, v[28:29], off offset:2048
	v_add_co_u32_e32 v28, vcc, s7, v8
	s_mov_b32 s7, 0xf000
	s_nop 0
	v_addc_co_u32_e32 v29, vcc, 0, v9, vcc
	v_add_co_u32_e32 v30, vcc, s7, v8
	s_mov_b32 s7, 0x14000
	s_nop 0
	v_addc_co_u32_e32 v31, vcc, 0, v9, vcc
	global_load_ushort v63, v[30:31], off offset:2048
	v_add_co_u32_e32 v30, vcc, s7, v8
	s_mov_b32 s7, 0x16000
	s_nop 0
	v_addc_co_u32_e32 v31, vcc, 0, v9, vcc
	v_add_co_u32_e32 v32, vcc, s7, v8
	s_mov_b32 s7, 0x1b000
	s_nop 0
	v_addc_co_u32_e32 v33, vcc, 0, v9, vcc
	global_load_ushort v65, v[32:33], off offset:2048
	v_add_co_u32_e32 v32, vcc, s7, v8
	s_mov_b32 s7, 0x1d000
	s_nop 0
	v_addc_co_u32_e32 v33, vcc, 0, v9, vcc
	v_add_co_u32_e32 v34, vcc, s7, v8
	s_mov_b32 s7, 0x22000
	s_nop 0
	v_addc_co_u32_e32 v35, vcc, 0, v9, vcc
	global_load_ushort v67, v[34:35], off offset:2048
	v_add_co_u32_e32 v34, vcc, s7, v8
	s_mov_b32 s95, 0x24000
	s_nop 0
	v_addc_co_u32_e32 v35, vcc, 0, v9, vcc
	v_add_co_u32_e32 v36, vcc, s95, v8
	s_mov_b32 s96, 0x29000
	s_nop 0
	v_addc_co_u32_e32 v37, vcc, 0, v9, vcc
	global_load_ushort v69, v[36:37], off offset:2048
	v_add_co_u32_e32 v36, vcc, s96, v8
	s_mov_b32 s97, 0x2b000
	s_nop 0
	v_addc_co_u32_e32 v37, vcc, 0, v9, vcc
	v_add_co_u32_e32 v38, vcc, s97, v8
	s_mov_b32 s34, 0x30000
	s_nop 0
	v_addc_co_u32_e32 v39, vcc, 0, v9, vcc
	global_load_ushort v93, v[38:39], off offset:2048
	v_add_co_u32_e32 v38, vcc, s34, v8
	s_mov_b32 s35, 0x32000
	s_nop 0
	v_addc_co_u32_e32 v39, vcc, 0, v9, vcc
	v_add_co_u32_e32 v40, vcc, s35, v8
	s_mov_b32 s88, 0x37000
	s_nop 0
	v_addc_co_u32_e32 v41, vcc, 0, v9, vcc
	global_load_ushort v66, v[32:33], off offset:-4096
	global_load_ushort v68, v[34:35], off offset:-4096
	global_load_ushort v92, v[36:37], off offset:-4096
	global_load_ushort v94, v[38:39], off offset:-4096
	global_load_ushort v96, v[40:41], off offset:2048
	v_add_co_u32_e32 v40, vcc, s88, v8
	global_load_ushort v23, v[4:5], off
	global_load_ushort v53, v[6:7], off
	global_load_ushort v55, v[16:17], off
	global_load_ushort v57, v[18:19], off
	global_load_ushort v60, v[26:27], off offset:-4096
	global_load_ushort v62, v[28:29], off offset:-4096
	global_load_ushort v64, v[30:31], off offset:-4096
	global_load_ushort v51, v[2:3], off
	v_addc_co_u32_e32 v41, vcc, 0, v9, vcc
	global_load_ushort v8, v[40:41], off offset:-4096
	global_load_ushort v9, v[10:11], off offset:2048
	s_nop 0
	global_load_ushort v10, v[26:27], off
	global_load_ushort v226, v[14:15], off offset:2048
	global_load_ushort v227, v[28:29], off
	global_load_ushort v228, v[4:5], off offset:2048
	global_load_ushort v229, v[30:31], off
	global_load_ushort v230, v[12:13], off offset:2048
	global_load_ushort v231, v[32:33], off
	global_load_ushort v232, v[2:3], off offset:2048
	global_load_ushort v233, v[34:35], off
	global_load_ushort v234, v[6:7], off offset:2048
	global_load_ushort v235, v[36:37], off
	global_load_ushort v236, v[16:17], off offset:2048
	global_load_ushort v237, v[38:39], off
	global_load_ushort v238, v[18:19], off offset:2048
	global_load_ushort v239, v[40:41], off
	s_ashr_i32 s7, s6, 31
	s_lshl_b64 s[6:7], s[6:7], 15
	s_add_u32 s6, s4, s6
	s_addc_u32 s7, s5, s7
	v_mov_b32_e32 v77, v75
	s_movk_i32 s86, 0x4000
	v_mov_b32_e32 v79, v75
	v_mov_b32_e32 v81, v75
	s_add_u32 s48, s76, 0x506e8000
	s_mov_b32 s12, 0xf400
	s_addc_u32 s49, s77, 0
	s_add_u32 s54, s76, 0x546e8000
	v_readlane_b32 s13, v254, 10
	s_addc_u32 s55, s77, 0
	s_bfe_u32 s20, s13, 0x20006
	v_readlane_b32 s31, v254, 12
	s_movk_i32 s29, 0x110
	s_lshr_b32 s21, s13, 7
	s_and_b32 s22, s21, 0x1fffffe
	s_movk_i32 s28, 0x90
	s_mov_b32 s73, 0x5040100
	s_movk_i32 s8, 0x17f
	s_movk_i32 s10, 0x1ff
	s_waitcnt vmcnt(46)
	v_perm_b32 v160, v20, v1, s73
	v_mov_b32_e32 v1, 0x8487b800
	s_mov_b32 s66, 0x3a800000
	v_and_b32_e32 v71, 48, v72
	s_mov_b32 s43, 0
	v_cmp_lt_u32_e64 s[8:9], s8, v0
	v_cmp_lt_u32_e64 s[10:11], s10, v0
	s_waitcnt vmcnt(44)
	v_perm_b32 v159, v22, v21, s73
	s_waitcnt vmcnt(41)
	v_perm_b32 v157, v50, v25, s73
	s_movk_i32 s74, 0xd800
	s_brev_b32 s67, 60
	s_mov_b32 s75, 0x800000
	s_mov_b32 s89, 0x42fe0000
	s_mov_b32 s90, 0x40c0c00
	v_mov_b32_e32 v131, 0x8a88b000
	s_mov_b32 s91, 0
	v_mov_b32_e32 v133, v75
	v_mov_b32_e32 v135, v75
	v_mov_b32_e32 v137, v75
	v_mov_b32_e32 v139, v75
	v_mov_b32_e32 v141, v75
	v_mov_b32_e32 v143, v75
	v_mov_b32_e32 v145, v75
	v_mov_b32_e32 v147, v75
	v_mov_b32_e32 v132, v75
	v_mov_b32_e32 v134, v75
	v_mov_b32_e32 v136, v75
	v_mov_b32_e32 v138, v75
	v_mov_b32_e32 v140, v75
	v_mov_b32_e32 v142, v75
	v_mov_b32_e32 v144, v75
	v_mov_b32_e32 v146, v75
	s_waitcnt vmcnt(29)
	v_perm_b32 v149, v66, v65, s73
	s_waitcnt vmcnt(28)
	v_perm_b32 v148, v68, v67, s73
	s_waitcnt vmcnt(27)
	v_perm_b32 v69, v92, v69, s73
	s_waitcnt vmcnt(26)
	v_perm_b32 v68, v94, v93, s73
	v_lshl_or_b32 v92, v190, 3, v1
	v_mov_b32_e32 v93, v75
	v_lshlrev_b32_e32 v94, 4, v190
	s_waitcnt vmcnt(24)
	v_perm_b32 v158, v24, v23, s73
	s_waitcnt vmcnt(23)
	v_perm_b32 v155, v54, v53, s73
	s_waitcnt vmcnt(22)
	v_perm_b32 v154, v56, v55, s73
	s_waitcnt vmcnt(21)
	v_perm_b32 v153, v58, v57, s73
	s_waitcnt vmcnt(20)
	v_perm_b32 v152, v60, v59, s73
	s_waitcnt vmcnt(19)
	v_perm_b32 v151, v62, v61, s73
	s_waitcnt vmcnt(18)
	v_perm_b32 v150, v64, v63, s73
	s_waitcnt vmcnt(17)
	v_perm_b32 v156, v52, v51, s73
	s_waitcnt vmcnt(16)
	v_perm_b32 v67, v8, v96, s73
	v_mov_b32_e32 v1, v75
	s_waitcnt vmcnt(14)
	v_lshl_or_b32 v26, v10, 16, v9
	s_nop 0
	s_nop 0
	v_mov_b32_e32 v8, v75
	s_waitcnt vmcnt(12)
	v_lshl_or_b32 v27, v227, 16, v226
	s_waitcnt vmcnt(10)
	v_lshl_or_b32 v28, v229, 16, v228
	s_nop 0
	s_nop 0
	v_lshlrev_b32_e32 v9, 4, v0
	v_and_b32_e32 v74, 0xf0, v9
	v_and_b32_e32 v76, 0x1f00, v9
	v_add_u32_e32 v13, 0, v74
	v_lshl_add_u64 v[82:83], s[4:5], 0, v[74:75]
	s_lshl_b32 s4, s31, 4
	s_and_b32 s42, s4, 0x3fffffc0
	s_or_b32 s64, s4, 48
	s_add_i32 s4, 0, 0x17c00
	s_cmp_le_u32 s22, s20
	s_cselect_b64 s[56:57], -1, 0
	s_lshl_b32 s87, s22, 5
	s_or_b32 s30, s21, 1
	v_and_b32_e32 v10, 0x70, v9
	v_lshl_add_u32 v85, v0, 2, s4
	v_lshl_add_u32 v87, v70, 2, s4
	s_movk_i32 s4, 0x80
	v_cmp_gt_u32_e64 s[4:5], s4, v0
	s_waitcnt vmcnt(8)
	v_lshl_or_b32 v29, v231, 16, v230
	s_waitcnt vmcnt(6)
	v_lshl_or_b32 v30, v233, 16, v232
	v_mov_b32_e32 v6, 0x2000
	s_waitcnt vmcnt(4)
	v_lshl_or_b32 v31, v235, 16, v234
	s_waitcnt vmcnt(2)
	v_lshl_or_b32 v32, v237, 16, v236
	s_waitcnt vmcnt(0)
	v_lshl_or_b32 v33, v239, 16, v238
	v_lshl_add_u64 v[2:3], s[6:7], 0, v[74:75]
	v_lshl_add_u64 v[4:5], v[2:3], 0, v[76:77]
	global_load_dwordx4 v[34:37], v[4:5], off
	v_add_co_u32_e32 v4, vcc, s86, v4
	s_movk_i32 s6, 0x3f00
	s_nop 0
	v_addc_co_u32_e32 v5, vcc, 0, v5, vcc
	v_bitop3_b32 v78, v9, s6, v6 bitop3:0xc8
	global_load_dwordx4 v[42:45], v[4:5], off
	s_movk_i32 s6, 0x7f00
	v_mov_b32_e32 v4, 0x6000
	v_bitop3_b32 v80, v9, s6, v4 bitop3:0xc8
	v_lshl_add_u64 v[6:7], v[2:3], 0, v[78:79]
	v_lshl_add_u64 v[2:3], v[2:3], 0, v[80:81]
	global_load_dwordx4 v[38:41], v[6:7], off
	global_load_dwordx4 v[46:49], v[2:3], off
	v_lshrrev_b32_e32 v4, 7, v0
	v_mul_u32_u24_e32 v5, 0x880, v4
	v_lshlrev_b32_e32 v11, 5, v4
	v_lshrrev_b32_e32 v4, 4, v0
	v_mul_u32_u24_e32 v4, 0x110, v4
	v_add3_u32 v95, v13, v4, s12
	v_or_b32_e32 v4, 0x200, v0
	v_lshrrev_b32_e32 v4, 4, v4
	v_and_b32_e32 v2, 15, v0
	v_mul_u32_u24_e32 v14, 0x110, v4
	v_or_b32_e32 v4, 0x600, v0
	v_lshrrev_b32_e32 v3, 4, v190
	v_lshl_or_b32 v84, s20, 4, v2
	v_lshrrev_b32_e32 v4, 4, v4
	v_lshlrev_b32_e32 v12, 2, v3
	v_mul_u32_u24_e32 v15, 0x110, v4
	v_lshlrev_b32_e32 v99, 3, v3
	v_and_b32_e32 v3, 48, v190
	v_mad_u32_u24 v4, v84, s29, 0
	v_add_u32_e32 v16, 0, v3
	v_add_u32_e32 v109, v4, v3
	v_lshlrev_b32_e32 v3, 7, v84
	v_sub_u32_e32 v3, v4, v3
	s_lshl_b32 s12, s22, 4
	v_add_u32_e32 v114, v3, v99
	v_or_b32_e32 v3, s12, v2
	v_mul_lo_u32 v17, v3, s29
	v_or_b32_e32 v3, s12, v12
	s_cmp_le_u32 s30, s20
	v_cmp_gt_u32_e64 s[12:13], v3, v84
	v_cmp_lt_u32_e64 s[14:15], v3, v84
	v_or_b32_e32 v4, 2, v3
	v_or_b32_e32 v3, 3, v3
	s_cselect_b64 s[58:59], -1, 0
	s_lshl_b32 s20, s30, 4
	v_cmp_gt_u32_e64 s[18:19], v3, v84
	v_or_b32_e32 v3, s20, v2
	v_mul_lo_u32 v18, v3, s29
	v_or_b32_e32 v3, s20, v12
	v_cmp_gt_u32_e64 s[16:17], v4, v84
	v_cmp_gt_u32_e64 s[20:21], v3, v84
	v_cmp_lt_u32_e64 s[22:23], v3, v84
	v_or_b32_e32 v4, 2, v3
	v_or_b32_e32 v3, 3, v3
	v_or_b32_e32 v5, v5, v70
	v_cmp_gt_u32_e64 s[26:27], v3, v84
	s_lshl_b32 s70, s30, 5
	v_or_b32_e32 v3, s42, v2
	s_add_i32 s30, 0, 0x18400
	v_lshl_add_u32 v89, v5, 1, 0
	v_mad_u32_u24 v9, v70, s28, 0
	v_cmp_gt_u32_e64 s[24:25], v4, v84
	v_or_b32_e32 v4, 16, v3
	v_or_b32_e32 v5, 32, v3
	v_or_b32_e32 v2, s64, v2
	v_lshl_add_u32 v115, v84, 3, s30
	s_and_b32 s30, s31, 0x3fffffc
	v_lshlrev_b32_e32 v74, 2, v10
	s_movk_i32 s6, 0xff
	v_mul_lo_u32 v19, v3, s28
	v_mul_lo_u32 v97, v4, s28
	v_mul_lo_u32 v98, v5, s28
	v_mul_lo_u32 v100, v2, s28
	v_mul_lo_u32 v101, v3, s29
	v_mul_lo_u32 v102, v4, s29
	v_mul_lo_u32 v103, v5, s29
	v_mul_lo_u32 v104, v2, s29
	v_lshl_add_u64 v[90:91], s[36:37], 0, v[74:75]
	s_add_u32 s36, s76, 0x8688b000
	v_add_u32_e32 v117, v9, v11
	v_mbcnt_lo_u32_b32 v9, -1, 0
	v_cmp_lt_u32_e64 s[6:7], s6, v0
	v_cmp_gt_u32_e64 s[28:29], 16, v190
	v_add_u32_e32 v116, s30, v115
	v_or_b32_e32 v86, s42, v12
	v_or_b32_e32 v88, s64, v12
	s_addc_u32 s37, s77, 0
	s_lshl_b32 s71, s31, 3
	v_cmp_eq_u32_e64 s[30:31], 0, v190
	v_mov_b32_e32 v2, v75
	v_mov_b32_e32 v4, v75
	v_mov_b32_e32 v3, v75
	v_mov_b32_e32 v6, v75
	v_mov_b32_e32 v5, v75
	v_mov_b32_e32 v7, v75
	v_lshlrev_b32_e32 v74, 1, v10
	v_lshlrev_b32_e32 v96, 1, v12
	s_lshl_b32 s60, s42, 1
	s_lshl_b32 s64, s64, 1
	v_add_u32_e32 v118, v13, v14
	v_add_u32_e32 v119, v13, v15
	v_add_u32_e32 v120, v16, v17
	v_add_u32_e32 v121, v16, v18
	v_add_u32_e32 v122, v16, v19
	v_add_u32_e32 v123, v16, v97
	v_add_u32_e32 v124, v16, v98
	v_add_u32_e32 v125, v16, v100
	v_add_u32_e32 v126, v16, v101
	v_add_u32_e32 v127, v16, v102
	v_add_u32_e32 v128, v16, v103
	v_add_u32_e32 v129, v16, v104
	v_mbcnt_hi_u32_b32 v130, -1, v9
	v_mov_b32_e32 v98, 0x358637bd
	s_and_b32 s98, s61, 0x380
	v_or_b32_e32 v252, s98, v70
	v_lshlrev_b32_e32 v252, 2, v252
	global_load_dword v250, v252, s[38:39]
	v_add_u32_e32 v252, 0x1000, v252
	global_load_dword v251, v252, s[38:39]
	s_waitcnt vmcnt(0)
	s_branch .LBB0_524

.LBB0_526:
	s_ashr_i32 s80, s61, 10
	s_ashr_i32 s81, s80, 31
	s_lshl_b32 s42, s61, 6
	s_lshl_b64 s[82:83], s[80:81], 13
	s_and_b32 s94, s42, 0x1fc0
	s_or_b32 s65, s82, s94
	v_or_b32_e32 v108, s65, v84
	v_mov_b64_e32 v[102:103], s[76:77]
	s_and_b32 s84, s61, 0x380
	v_mad_u64_u32 v[110:111], vcc, v108, s3, v[102:103]
	v_mov_b32_e32 v101, s83
	v_or_b32_e32 v100, s65, v72
	s_lshl_b32 s42, s84, 1
	v_mad_i32_i24 v111, s83, v73, v111
	v_lshlrev_b64 v[50:51], 12, v[100:101]
	v_lshl_add_u64 v[102:103], v[110:111], 0, s[42:43]
	v_mov_b32_e32 v97, v75
	v_lshl_add_u64 v[50:51], s[48:49], 0, v[50:51]
	v_mov_b32_e32 v9, s83
	v_lshl_add_u64 v[102:103], v[102:103], 0, v[96:97]
	s_mov_b64 s[82:83], 0x364eb000
	v_or_b32_e32 v66, s84, v70
	v_lshl_add_u64 v[50:51], v[50:51], 0, s[42:43]
	v_lshlrev_b64 v[58:59], 5, v[100:101]
	v_lshl_add_u64 v[102:103], v[102:103], 0, s[82:83]
	s_mov_b32 s61, s43
	v_lshlrev_b32_e32 v162, 2, v66
	v_mov_b32_e32 v163, v75
	v_lshl_add_u64 v[54:55], v[50:51], 0, v[74:75]
	v_lshl_add_u64 v[62:63], s[54:55], 0, v[58:59]
	v_lshl_add_u64 v[104:105], v[102:103], 0, s[60:61]
	v_lshl_add_u64 v[164:165], s[38:39], 0, v[162:163]
	global_load_dwordx4 v[50:53], v[54:55], off offset:16
	s_nop 0
	global_load_dwordx4 v[54:57], v[54:55], off
	s_nop 0
	global_load_dwordx4 v[58:61], v[62:63], off offset:16
	s_nop 0
	global_load_dwordx4 v[62:65], v[62:63], off
	s_nop 0
	global_load_dwordx2 v[112:113], v[104:105], off
	global_load_dwordx2 v[106:107], v[104:105], off offset:32
	s_nop 0
	global_load_dwordx2 v[104:105], v[104:105], off offset:64
	s_mov_b32 s65, s43
	v_mov_b32_e32 v66, v250
	v_add_co_u32_e32 v162, vcc, s72, v164
	v_lshl_add_u64 v[102:103], v[102:103], 0, s[64:65]
	s_nop 0
	v_addc_co_u32_e32 v163, vcc, 0, v165, vcc
	v_mov_b32_e32 v97, v251
	s_andn2_b64 vcc, exec, s[56:57]
	global_load_dwordx2 v[102:103], v[102:103], off
	s_cmp_lg_u64 s[68:69], 0
	s_cbranch_scc1 .Lp5pf_done
	s_ashr_i32 s100, s92, 10
	s_lshl_b32 s98, s92, 6
	s_ashr_i32 s101, s100, 31
	s_and_b32 s98, s98, 0x1fc0
	s_lshl_b64 s[100:101], s[100:101], 13
	v_or_b32_e32 v252, s98, v71
	v_or_b32_e32 v252, s100, v252
	v_mov_b64_e32 v[250:251], s[0:1]
	s_and_b32 s98, s92, 0x380
	s_lshl_b32 s98, s98, 1
	s_addk_i32 s98, 0x2000
	s_mov_b32 s99, 0
	v_mad_u64_u32 v[250:251], s[82:83], v252, s3, v[250:251]
	v_lshlrev_b32_e32 v226, 1, v70
	v_mov_b32_e32 v227, v75
	v_mad_i32_i24 v251, s101, v73, v251
	v_lshl_add_u64 v[226:227], v[226:227], 0, s[98:99]
	s_ashr_i32 s101, s92, 31
	s_mov_b32 s100, s92
	v_lshl_add_u64 v[250:251], v[250:251], 0, v[226:227]
	s_lshl_b64 s[100:101], s[100:101], 15
	s_movk_i32 s98, 0x3800
	global_load_ushort v234, v[250:251], off offset:-2048
	global_load_ushort v226, v[250:251], off
	global_load_ushort v242, v[250:251], off offset:2048
	v_lshl_add_u64 v[250:251], v[250:251], 0, s[98:99]
	global_load_ushort v132, v[250:251], off offset:-2048
	global_load_ushort v133, v[250:251], off
	global_load_ushort v2, v[250:251], off offset:2048
	v_lshl_add_u64 v[250:251], v[250:251], 0, s[98:99]
	global_load_ushort v235, v[250:251], off offset:-2048
	global_load_ushort v227, v[250:251], off
	global_load_ushort v243, v[250:251], off offset:2048
	v_lshl_add_u64 v[250:251], v[250:251], 0, s[98:99]
	global_load_ushort v134, v[250:251], off offset:-2048
	global_load_ushort v135, v[250:251], off
	global_load_ushort v1, v[250:251], off offset:2048
	v_lshl_add_u64 v[250:251], v[250:251], 0, s[98:99]
	global_load_ushort v236, v[250:251], off offset:-2048
	global_load_ushort v228, v[250:251], off
	global_load_ushort v244, v[250:251], off offset:2048
	v_lshl_add_u64 v[250:251], v[250:251], 0, s[98:99]
	global_load_ushort v136, v[250:251], off offset:-2048
	global_load_ushort v137, v[250:251], off
	global_load_ushort v4, v[250:251], off offset:2048
	v_lshl_add_u64 v[250:251], v[250:251], 0, s[98:99]
	global_load_ushort v237, v[250:251], off offset:-2048
	global_load_ushort v229, v[250:251], off
	global_load_ushort v245, v[250:251], off offset:2048
	v_lshl_add_u64 v[250:251], v[250:251], 0, s[98:99]
	global_load_ushort v138, v[250:251], off offset:-2048
	global_load_ushort v139, v[250:251], off
	global_load_ushort v3, v[250:251], off offset:2048
	v_lshl_add_u64 v[250:251], v[250:251], 0, s[98:99]
	global_load_ushort v238, v[250:251], off offset:-2048
	global_load_ushort v230, v[250:251], off
	global_load_ushort v246, v[250:251], off offset:2048
	v_lshl_add_u64 v[250:251], v[250:251], 0, s[98:99]
	global_load_ushort v140, v[250:251], off offset:-2048
	global_load_ushort v141, v[250:251], off
	global_load_ushort v6, v[250:251], off offset:2048
	v_lshl_add_u64 v[250:251], v[250:251], 0, s[98:99]
	global_load_ushort v239, v[250:251], off offset:-2048
	global_load_ushort v231, v[250:251], off
	global_load_ushort v247, v[250:251], off offset:2048
	v_lshl_add_u64 v[250:251], v[250:251], 0, s[98:99]
	global_load_ushort v142, v[250:251], off offset:-2048
	global_load_ushort v143, v[250:251], off
	global_load_ushort v5, v[250:251], off offset:2048
	v_lshl_add_u64 v[250:251], v[250:251], 0, s[98:99]
	global_load_ushort v240, v[250:251], off offset:-2048
	global_load_ushort v232, v[250:251], off
	global_load_ushort v248, v[250:251], off offset:2048
	v_lshl_add_u64 v[250:251], v[250:251], 0, s[98:99]
	global_load_ushort v144, v[250:251], off offset:-2048
	global_load_ushort v145, v[250:251], off
	global_load_ushort v8, v[250:251], off offset:2048
	v_lshl_add_u64 v[250:251], v[250:251], 0, s[98:99]
	global_load_ushort v241, v[250:251], off offset:-2048
	global_load_ushort v233, v[250:251], off
	global_load_ushort v249, v[250:251], off offset:2048
	v_lshl_add_u64 v[250:251], v[250:251], 0, s[98:99]
	global_load_ushort v146, v[250:251], off offset:-2048
	global_load_ushort v147, v[250:251], off
	global_load_ushort v7, v[250:251], off offset:2048
	v_lshl_add_u64 v[10:11], v[82:83], 0, s[100:101]
	s_mov_b32 s100, s86
	s_mov_b32 s101, 0
	v_lshl_add_u64 v[14:15], v[10:11], 0, v[78:79]
	v_lshl_add_u64 v[22:23], v[10:11], 0, v[80:81]
	v_lshl_add_u64 v[10:11], v[10:11], 0, v[76:77]
	v_lshl_add_u64 v[18:19], v[10:11], 0, s[100:101]
	global_load_dwordx4 v[22:25], v[22:23], off
	global_load_dwordx4 v[14:17], v[14:15], off
	global_load_dwordx4 v[18:21], v[18:19], off
	global_load_dwordx4 v[10:13], v[10:11], off
	s_and_b32 s98, s92, 0x380
	v_or_b32_e32 v252, s98, v70
	v_lshlrev_b32_e32 v252, 2, v252
	global_load_dword v250, v252, s[38:39]
	v_add_u32_e32 v252, 0x1000, v252
	global_load_dword v251, v252, s[38:39]

.LBB0_532:
	s_or_b64 exec, exec, s[82:83]
	s_lshl_b32 s82, s84, 2
	s_add_u32 s84, s40, s82
	s_addc_u32 s85, s41, 0
	v_lshlrev_b32_e32 v45, 2, v86
	s_waitcnt lgkmcnt(0)
	s_barrier
	s_cmp_lg_u64 s[68:69], 0
	s_cbranch_scc1 .Lp5own_w0
	s_waitcnt vmcnt(54)
	s_branch .Lp5own_w1

.Lp5own_w1:
	global_load_dwordx4 v[66:69], v45, s[84:85]
	s_mov_b32 s83, s43
	global_load_dwordx4 v[194:197], v45, s[84:85] offset:64
	global_load_dwordx4 v[198:201], v45, s[84:85] offset:128
	v_lshlrev_b32_e32 v206, 2, v88
	global_load_dwordx4 v[202:205], v206, s[84:85]
	v_lshl_add_u64 v[208:209], v[90:91], 0, s[82:83]
	global_load_dwordx4 v[210:213], v[208:209], off
	global_load_dwordx4 v[214:217], v[208:209], off offset:16
	global_load_dwordx4 v[218:221], v[208:209], off offset:32
	global_load_dwordx4 v[222:225], v[208:209], off offset:48
	ds_read_b64 v[42:43], v115
	v_mad_u64_u32 v[46:47], vcc, v108, s74, v[110:111]
	v_mov_b32_e32 v154, v63
	v_mov_b32_e32 v155, v64
	v_mov_b32_e32 v63, v65
	v_lshlrev_b32_e32 v110, 16, v112
	v_mov_b32_e32 v64, v60
	v_mov_b32_e32 v65, v58
	v_mov_b32_e32 v58, v61
	v_mov_b32_e32 v60, v47
	v_pk_add_f32 v[62:63], v[154:155], v[62:63]
	v_mul_f32_e32 v47, 0xbfb8aa3b, v110
	v_pk_add_f32 v[58:59], v[64:65], v[58:59]
	v_mad_u64_u32 v[60:61], vcc, v9, s74, v[60:61]
	v_pk_add_f32 v[62:63], v[62:63], v[62:63] op_sel:[0,1] op_sel_hi:[1,0]
	v_exp_f32_e32 v9, v47
	v_sub_u32_e32 v47, v60, v108
	v_pk_add_f32 v[60:61], v[62:63], v[58:59] op_sel:[0,1] op_sel_hi:[1,0]
	s_waitcnt lgkmcnt(0)
	v_mov_b32_e32 v59, v42
	v_mov_b32_e32 v61, v43
	v_lshlrev_b32_e32 v148, 16, v113
	v_pk_add_f32 v[42:43], v[58:59], v[60:61]
	v_and_b32_e32 v112, 0xffff0000, v112
	v_and_b32_e32 v150, 0xffff0000, v113
	v_mul_f32_e32 v111, 0xbfb8aa3b, v148
	v_lshl_add_u64 v[46:47], v[46:47], 0, s[42:43]
	s_mov_b64 vcc, 0x8688b800
	v_pk_fma_f32 v[42:43], v[42:43], s[66:67], v[98:99] op_sel_hi:[1,1,0]
	v_mul_f32_e32 v97, 0xbfb8aa3b, v112
	v_mul_f32_e32 v113, 0xbfb8aa3b, v150
	v_exp_f32_e32 v65, v111
	v_lshl_add_u64 v[46:47], v[46:47], 0, vcc
	v_mul_f32_e32 v58, 0x4b800000, v43
	v_cmp_gt_f32_e32 vcc, s75, v43
	v_exp_f32_e32 v64, v97
	v_exp_f32_e32 v97, v113
	v_cndmask_b32_e32 v43, v43, v58, vcc
	v_rsq_f32_e32 v43, v43
	v_add_f32_e32 v9, 1.0, v9
	v_add_f32_e32 v62, 1.0, v65
	v_add_f32_e32 v63, 1.0, v64
	v_add_f32_e32 v64, 1.0, v97
	v_rcp_f32_e32 v60, v9
	v_rcp_f32_e32 v62, v62
	v_mul_f32_e32 v9, 0x45800000, v43
	v_cndmask_b32_e32 v9, v43, v9, vcc
	v_mul_f32_e32 v111, v38, v9
	v_mul_f32_e32 v149, v40, v9
	v_mul_f32_e32 v113, v39, v9
	v_mul_f32_e32 v151, v41, v9
	v_lshlrev_b32_e32 v152, 1, v86
	v_mov_b32_e32 v153, v75
	v_lshl_add_u64 v[58:59], v[46:47], 0, v[152:153]
	s_mov_b32 s83, s43
	v_cmp_gt_f32_e32 vcc, s75, v42
	s_waitcnt vmcnt(7)
	v_mov_b32_e32 v61, v66
	v_rcp_f32_e32 v66, v63
	v_mov_b32_e32 v63, v68
	v_rcp_f32_e32 v68, v64
	v_pk_mul_f32 v[38:39], v[60:61], v[110:111]
	v_pk_mul_f32 v[40:41], v[62:63], v[148:149]
	v_mul_f32_e32 v43, v38, v39
	v_mul_f32_e32 v60, v40, v41
	v_pk_mul_f32 v[38:39], v[66:67], v[112:113]
	v_pk_mul_f32 v[40:41], v[68:69], v[150:151]
	v_mul_f32_e32 v38, v38, v39
	v_mul_f32_e32 v39, v40, v41
	v_cvt_pk_bf16_f32 v38, v43, v38
	v_cvt_pk_bf16_f32 v39, v60, v39
	global_store_dwordx2 v[58:59], v[38:39], off
	v_lshlrev_b32_e32 v60, 16, v106
	v_and_b32_e32 v62, 0xffff0000, v106
	v_lshlrev_b32_e32 v64, 16, v107
	v_and_b32_e32 v66, 0xffff0000, v107
	v_mul_f32_e32 v43, 0xbfb8aa3b, v60
	v_mul_f32_e32 v61, 0xbfb8aa3b, v62
	v_mul_f32_e32 v63, 0xbfb8aa3b, v64
	v_mul_f32_e32 v65, 0xbfb8aa3b, v66
	v_exp_f32_e32 v43, v43
	v_exp_f32_e32 v61, v61
	v_exp_f32_e32 v63, v63
	v_exp_f32_e32 v65, v65
	v_add_f32_e32 v43, 1.0, v43
	v_add_f32_e32 v61, 1.0, v61
	v_add_f32_e32 v63, 1.0, v63
	v_add_f32_e32 v65, 1.0, v65
	v_rcp_f32_e32 v68, v43
	v_rcp_f32_e32 v106, v61
	v_rcp_f32_e32 v110, v63
	v_rcp_f32_e32 v112, v65
	v_mul_f32_e32 v61, v34, v9
	v_mul_f32_e32 v63, v35, v9
	v_mul_f32_e32 v65, v36, v9
	v_mul_f32_e32 v67, v37, v9
	v_lshlrev_b32_e32 v43, 2, v88
	s_waitcnt vmcnt(7)
	v_mov_b32_e32 v69, v194
	v_mov_b32_e32 v107, v195
	v_mov_b32_e32 v111, v196
	v_mov_b32_e32 v113, v197
	v_pk_mul_f32 v[34:35], v[68:69], v[60:61]
	v_pk_mul_f32 v[36:37], v[106:107], v[62:63]
	v_pk_mul_f32 v[38:39], v[110:111], v[64:65]
	v_pk_mul_f32 v[40:41], v[112:113], v[66:67]
	v_mul_f32_e32 v34, v34, v35
	v_mul_f32_e32 v35, v36, v37
	v_mul_f32_e32 v36, v38, v39
	v_mul_f32_e32 v37, v40, v41
	v_cvt_pk_bf16_f32 v34, v34, v35
	v_cvt_pk_bf16_f32 v35, v36, v37
	global_store_dwordx2 v[58:59], v[34:35], off offset:32
	v_lshlrev_b32_e32 v38, 16, v104
	v_and_b32_e32 v40, 0xffff0000, v104
	v_lshlrev_b32_e32 v60, 16, v105
	v_and_b32_e32 v62, 0xffff0000, v105
	v_mul_f32_e32 v39, 0xbfb8aa3b, v38
	v_mul_f32_e32 v41, 0xbfb8aa3b, v40
	v_mul_f32_e32 v45, 0xbfb8aa3b, v60
	v_mul_f32_e32 v61, 0xbfb8aa3b, v62
	v_exp_f32_e32 v39, v39
	v_exp_f32_e32 v41, v41
	v_exp_f32_e32 v45, v45
	v_exp_f32_e32 v61, v61
	v_add_f32_e32 v39, 1.0, v39
	v_add_f32_e32 v41, 1.0, v41
	v_add_f32_e32 v45, 1.0, v45
	v_add_f32_e32 v61, 1.0, v61
	v_rcp_f32_e32 v64, v39
	v_rcp_f32_e32 v66, v41
	v_rcp_f32_e32 v68, v45
	v_rcp_f32_e32 v104, v61
	v_mul_f32_e32 v65, v30, v9
	v_mul_f32_e32 v67, v31, v9
	v_mul_f32_e32 v69, v32, v9
	v_mul_f32_e32 v105, v33, v9
	v_and_b32_e32 v45, 0xffff0000, v54
	s_waitcnt vmcnt(7)
	v_mov_b32_e32 v39, v198
	v_mov_b32_e32 v41, v199
	v_mov_b32_e32 v61, v200
	v_mov_b32_e32 v63, v201
	v_pk_mul_f32 v[30:31], v[64:65], v[38:39]
	v_pk_mul_f32 v[32:33], v[66:67], v[40:41]
	v_pk_mul_f32 v[34:35], v[68:69], v[60:61]
	v_pk_mul_f32 v[36:37], v[104:105], v[62:63]
	v_mul_f32_e32 v30, v30, v31
	v_mul_f32_e32 v31, v32, v33
	v_mul_f32_e32 v32, v34, v35
	v_mul_f32_e32 v33, v36, v37
	v_cvt_pk_bf16_f32 v30, v30, v31
	v_cvt_pk_bf16_f32 v31, v32, v33
	global_store_dwordx2 v[58:59], v[30:31], off offset:64
	v_lshlrev_b32_e32 v34, 16, v102
	v_and_b32_e32 v36, 0xffff0000, v102
	v_lshlrev_b32_e32 v38, 16, v103
	v_and_b32_e32 v40, 0xffff0000, v103
	v_mul_f32_e32 v35, 0xbfb8aa3b, v34
	v_mul_f32_e32 v37, 0xbfb8aa3b, v36
	v_mul_f32_e32 v39, 0xbfb8aa3b, v38
	v_mul_f32_e32 v41, 0xbfb8aa3b, v40
	v_exp_f32_e32 v35, v35
	v_exp_f32_e32 v37, v37
	v_exp_f32_e32 v39, v39
	v_exp_f32_e32 v41, v41
	v_lshlrev_b32_e32 v58, 1, v88
	v_mov_b32_e32 v59, v75
	v_add_f32_e32 v35, 1.0, v35
	v_add_f32_e32 v37, 1.0, v37
	v_add_f32_e32 v39, 1.0, v39
	v_add_f32_e32 v41, 1.0, v41
	v_lshl_add_u64 v[46:47], v[46:47], 0, v[58:59]
	v_rcp_f32_e32 v58, v35
	v_rcp_f32_e32 v62, v37
	v_rcp_f32_e32 v64, v39
	v_rcp_f32_e32 v66, v41
	v_mul_f32_e32 v59, v26, v9
	v_mul_f32_e32 v63, v27, v9
	v_mul_f32_e32 v65, v28, v9
	v_mul_f32_e32 v67, v29, v9
	v_lshl_add_u64 v[60:61], v[90:91], 0, s[82:83]
	v_mul_f32_e32 v43, 0x4b800000, v42
	v_cndmask_b32_e32 v42, v42, v43, vcc
	s_waitcnt vmcnt(7)
	v_mov_b32_e32 v35, v202
	v_mov_b32_e32 v37, v203
	v_mov_b32_e32 v39, v204
	v_mov_b32_e32 v41, v205
	v_pk_mul_f32 v[26:27], v[58:59], v[34:35]
	v_pk_mul_f32 v[28:29], v[62:63], v[36:37]
	v_pk_mul_f32 v[30:31], v[64:65], v[38:39]
	v_pk_mul_f32 v[32:33], v[66:67], v[40:41]
	v_mul_f32_e32 v9, v26, v27
	v_mul_f32_e32 v26, v28, v29
	v_mul_f32_e32 v27, v30, v31
	v_mul_f32_e32 v28, v32, v33
	v_cvt_pk_bf16_f32 v26, v9, v26
	v_cvt_pk_bf16_f32 v27, v27, v28
	global_store_dwordx2 v[46:47], v[26:27], off
	v_rsq_f32_e32 v64, v42
	v_lshlrev_b64 v[46:47], 11, v[100:101]
	v_lshl_add_u64 v[46:47], v[46:47], 1, s[36:37]
	v_lshl_add_u64 v[46:47], v[46:47], 0, s[42:43]
	v_lshl_add_u64 v[42:43], v[46:47], 0, v[74:75]
	v_mul_f32_e32 v46, 0x45800000, v64
	v_cndmask_b32_e32 v46, v64, v46, vcc
	v_lshlrev_b32_e32 v9, 16, v54
	v_lshlrev_b32_e32 v54, 16, v55
	v_and_b32_e32 v55, 0xffff0000, v55
	v_lshlrev_b32_e32 v58, 16, v56
	v_and_b32_e32 v56, 0xffff0000, v56
	v_lshlrev_b32_e32 v59, 16, v57
	v_and_b32_e32 v57, 0xffff0000, v57
	v_lshlrev_b32_e32 v60, 16, v50
	s_and_b32 s42, s91, 7
	v_and_b32_e32 v50, 0xffff0000, v50
	v_lshlrev_b32_e32 v61, 16, v51
	v_and_b32_e32 v51, 0xffff0000, v51
	v_lshlrev_b32_e32 v62, 16, v52
	v_and_b32_e32 v52, 0xffff0000, v52
	v_lshlrev_b32_e32 v63, 16, v53
	v_and_b32_e32 v53, 0xffff0000, v53
	s_cmp_lg_u32 s42, 7
	s_waitcnt vmcnt(7)
	v_pk_mul_f32 v[28:29], v[46:47], v[212:213] op_sel_hi:[0,1]
	v_pk_mul_f32 v[26:27], v[46:47], v[210:211] op_sel_hi:[0,1]
	s_waitcnt vmcnt(6)
	v_pk_mul_f32 v[30:31], v[46:47], v[214:215] op_sel_hi:[0,1]
	v_pk_mul_f32 v[32:33], v[46:47], v[216:217] op_sel_hi:[0,1]
	s_waitcnt vmcnt(5)
	v_pk_mul_f32 v[34:35], v[46:47], v[218:219] op_sel_hi:[0,1]
	v_mul_f32_e32 v9, v26, v9
	v_mul_f32_e32 v26, v27, v45
	v_mul_f32_e32 v27, v28, v54
	v_mul_f32_e32 v28, v29, v55
	v_mul_f32_e32 v29, v30, v58
	v_pk_mul_f32 v[36:37], v[46:47], v[220:221] op_sel_hi:[0,1]
	s_waitcnt vmcnt(4)
	v_pk_mul_f32 v[40:41], v[46:47], v[224:225] op_sel_hi:[0,1]
	v_pk_mul_f32 v[38:39], v[46:47], v[222:223] op_sel_hi:[0,1]
	v_mul_f32_e32 v30, v31, v56
	v_mul_f32_e32 v31, v32, v59
	v_mul_f32_e32 v32, v33, v57
	v_mul_f32_e32 v33, v34, v60
	v_cvt_pk_bf16_f32 v26, v9, v26
	v_cvt_pk_bf16_f32 v27, v27, v28
	v_cvt_pk_bf16_f32 v28, v29, v30
	v_cvt_pk_bf16_f32 v29, v31, v32
	v_mul_f32_e32 v34, v35, v50
	v_mul_f32_e32 v35, v36, v61
	v_mul_f32_e32 v36, v37, v51
	v_mul_f32_e32 v37, v38, v62
	v_mul_f32_e32 v38, v39, v52
	v_mul_f32_e32 v39, v40, v63
	v_mul_f32_e32 v40, v41, v53
	v_cvt_pk_bf16_f32 v30, v33, v34
	v_cvt_pk_bf16_f32 v31, v35, v36
	v_cvt_pk_bf16_f32 v32, v37, v38
	v_cvt_pk_bf16_f32 v33, v39, v40
	global_store_dwordx4 v[42:43], v[26:29], off
	global_store_dwordx4 v[42:43], v[30:33], off offset:16
	s_barrier
	s_cbranch_scc1 .LBB0_523
	v_xor_b32_e32 v9, 8, v130
	v_cmp_lt_i32_e32 vcc, v9, v44
	v_xor_b32_e32 v26, 4, v130
	s_add_i32 s42, s94, s71
	v_cndmask_b32_e32 v9, v130, v9, vcc
	v_cmp_lt_i32_e32 vcc, v26, v44
	s_lshl_b64 s[82:83], s[80:81], 24
	s_lshl_b64 s[84:85], s[42:43], 11
	v_cndmask_b32_e32 v26, v130, v26, vcc
	v_lshlrev_b32_e32 v50, 2, v26
	v_xor_b32_e32 v26, 2, v130
	s_add_u32 s82, s84, s82
	v_cmp_lt_i32_e32 vcc, v26, v44
	s_addc_u32 s83, s85, s83
	v_lshl_add_u64 v[42:43], s[82:83], 0, v[92:93]
	v_cndmask_b32_e32 v26, v130, v26, vcc
	s_lshl_b64 s[82:83], s[80:81], 25
	s_lshl_b64 s[84:85], s[42:43], 12
	v_lshlrev_b32_e32 v51, 2, v26
	v_xor_b32_e32 v26, 1, v130
	s_add_u32 s61, s84, s82
	v_cmp_lt_i32_e32 vcc, v26, v44
	s_addc_u32 s65, s85, s83
	s_lshl_b64 s[80:81], s[80:81], 15
	s_lshl_b32 s42, s42, 2
	v_cndmask_b32_e32 v26, v130, v26, vcc
	s_add_u32 s42, s80, s42
	v_lshlrev_b32_e32 v9, 2, v9
	v_lshlrev_b32_e32 v52, 2, v26
	v_mov_b32_e32 v45, s65
	v_or_b32_e32 v44, s61, v94
	s_addc_u32 s61, s81, 0
	s_mov_b32 s65, -2
	s_branch .LBB0_535
